# GLA scan pass B: the per-step vmcnt(0) waits counted down to vmcnt(12) (stores and next-step r loads stay in flight), r waited at its first use, decay-row DMA issued by every wave so the counts are wa
# baseline (speedup 1.0000x reference)
.LBB0_554:
	s_lshl_b32 s72, s22, 3
	s_add_i32 s90, s72, s20
	s_add_u32 s70, s70, s90
	s_addc_u32 s71, s71, 0
	s_lshl_b64 s[70:71], s[70:71], 11
	v_lshl_add_u64 v[66:67], v[198:199], 0, s[70:71]
	s_lshl_b32 s70, s84, 12
	s_lshl_b32 s84, s83, 6
	s_and_b32 s70, s70, 0x4000
	s_and_b32 s71, s84, 0xfffff800
	s_add_i32 s72, s86, s2
	s_add_i32 s71, s71, s70
	s_ashr_i32 s73, s72, 31
	v_or_b32_e32 v224, s71, v209
	s_lshl_b64 s[70:71], s[72:73], 10
	v_lshl_add_u64 v[226:227], v[210:211], 0, s[70:71]
	s_lshl_b64 s[70:71], s[72:73], 13
	v_lshl_add_u64 v[228:229], v[212:213], 0, s[70:71]
	s_lshl_b64 s[70:71], s[72:73], 15
	v_lshl_add_u64 v[230:231], v[214:215], 0, s[70:71]
	v_ashrrev_i32_e32 v225, 31, v224
	s_and_b32 s70, s81, 3
	v_lshlrev_b64 v[68:69], 12, v[224:225]
	s_lshl_b32 s71, s70, 10
	s_lshl_b32 s70, s22, 8
	v_lshl_add_u64 v[68:69], v[216:217], 0, v[68:69]
	s_or_b32 s22, s70, s71
	v_lshl_add_u64 v[232:233], s[22:23], 0, v[68:69]
	s_add_i32 s22, s20, s85
	s_lshl_b64 s[72:73], s[72:73], 16
	s_lshl_b64 s[88:89], s[22:23], 11
	s_add_u32 s22, s88, s72
	s_addc_u32 s71, s89, s73
	v_or_b32_e32 v234, s22, v196
	s_lshl_b32 s22, s87, 12
	s_and_b32 s85, s22, 0x4000
	s_lshl_b32 s2, s2, 6
	s_add_i32 s2, s85, s2
	global_load_dwordx4 v[78:81], v[66:67], off
	global_load_dwordx4 v[74:77], v[66:67], off offset:1024
	v_or_b32_e32 v66, s2, v209
	v_ashrrev_i32_e32 v67, 31, v66
	s_and_b32 s72, s83, 3
	v_lshlrev_b64 v[66:67], 12, v[66:67]
	v_lshl_add_u64 v[66:67], s[16:17], 0, v[66:67]
	s_lshl_b32 s22, s72, 10
	v_mov_b32_e32 v235, s71
	v_lshl_add_u64 v[66:67], v[66:67], 0, s[22:23]
	s_mov_b32 s71, s23
	v_lshl_add_u64 v[66:67], v[66:67], 0, s[70:71]
	v_lshl_add_u64 v[66:67], v[66:67], 0, s[30:31]
	v_lshl_add_u64 v[66:67], v[66:67], 0, v[194:195]
	v_add_co_u32_e32 v68, vcc, s53, v66
	global_load_dwordx2 v[122:123], v[66:67], off
	s_nop 0
	v_addc_co_u32_e32 v69, vcc, 0, v67, vcc
	global_load_dwordx2 v[236:237], v[68:69], off
	v_add_co_u32_e32 v68, vcc, s75, v66
	s_add_u32 s2, s16, s22
	s_nop 0
	v_addc_co_u32_e32 v69, vcc, 0, v67, vcc
	v_add_co_u32_e32 v66, vcc, s76, v66
	global_load_dwordx2 v[220:221], v[68:69], off
	s_nop 0
	v_addc_co_u32_e32 v67, vcc, 0, v67, vcc
	global_load_dwordx2 v[218:219], v[66:67], off
	s_addc_u32 s22, s17, 0
	s_add_u32 s2, s2, s70
	s_addc_u32 s22, s22, 0
	s_add_u32 s70, s2, s30
	s_addc_u32 s71, s22, 0
	s_lshl_b32 s2, s90, 2
	s_add_u32 s2, s3, s2
	v_lshl_add_u64 v[222:223], s[70:71], 0, v[194:195]
	s_addc_u32 s22, s4, 0
	s_lshl_b32 s70, s72, 7
	s_add_u32 s70, s2, s70
	s_mov_b32 s86, 0
	s_addc_u32 s71, s22, 0
	s_mov_b32 s2, 0
	s_waitcnt vmcnt(4)
.LBB0_555:
	s_add_i32 s22, s2, 1
	s_bitcmp1_b32 s22, 0
	s_cselect_b32 s72, 0x12400, 0
	s_add_i32 s72, s72, 0
	v_lshl_add_u64 v[66:67], s[14:15], 0, v[230:231]
	s_add_i32 s73, s72, s42
	v_lshl_add_u64 v[68:69], v[66:67], 0, s[34:35]
	s_mov_b32 m0, s73
	s_waitcnt vmcnt(12)
	s_waitcnt vmcnt(12) lgkmcnt(0)
	s_barrier
	global_load_lds_dwordx4 v[68:69], off
	v_lshl_add_u64 v[68:69], v[66:67], 0, s[36:37]
	s_add_i32 m0, s73, 0x8000
	s_add_i32 s73, s72, s48
	global_load_lds_dwordx4 v[68:69], off
	v_lshl_add_u64 v[68:69], v[66:67], 0, s[38:39]
	s_mov_b32 m0, s73
	s_and_b64 vcc, exec, s[10:11]
	global_load_lds_dwordx4 v[68:69], off
	v_lshl_add_u64 v[68:69], v[66:67], 0, s[40:41]
	s_add_i32 m0, s73, 0x8000
	s_add_i32 s73, s72, s50
	global_load_lds_dwordx4 v[68:69], off
	v_lshl_add_u64 v[68:69], v[66:67], 0, s[54:55]
	s_mov_b32 m0, s73
	s_nop 0
	global_load_lds_dwordx4 v[68:69], off
	v_lshl_add_u64 v[68:69], v[66:67], 0, s[56:57]
	s_add_i32 m0, s73, 0x8000
	s_add_i32 s73, s72, s52
	global_load_lds_dwordx4 v[68:69], off
	v_lshl_add_u64 v[68:69], v[66:67], 0, s[58:59]
	s_mov_b32 m0, s73
	v_lshl_add_u64 v[66:67], v[66:67], 0, s[60:61]
	global_load_lds_dwordx4 v[68:69], off
	s_add_i32 m0, s73, 0x8000
	s_add_i32 s73, s72, s33
	global_load_lds_dwordx4 v[66:67], off
	v_lshl_add_u64 v[66:67], s[14:15], 0, v[228:229]
	s_add_i32 m0, s73, 0x10000
	s_nop 0
	global_load_lds_dwordx4 v[66:67], off
	v_lshl_add_u64 v[66:67], s[14:15], 0, v[226:227]
	s_add_i32 m0, s72, 0x12000
	s_nop 0
	global_load_lds_dwordx4 v[66:67], off
.LBB0_557:
	v_lshl_add_u64 v[66:67], s[14:15], 0, v[234:235]
	v_add_co_u32_e32 v66, vcc, 0x3a010000, v66
	s_bitcmp1_b32 s2, 0
	s_nop 0
	v_addc_co_u32_e32 v67, vcc, 0, v67, vcc
	global_load_dwordx4 v[70:73], v[66:67], off
	s_nop 0
	global_load_dwordx4 v[66:69], v[66:67], off offset:1024
	s_cselect_b32 s2, 0x12400, 0
	s_add_i32 s2, s2, 0
	v_add_u32_e32 v247, s2, v196
	v_cvt_pk_bf16_f32 v82, v46, v47
	v_cvt_pk_bf16_f32 v83, v48, v49
	v_cvt_pk_bf16_f32 v84, v62, v63
	v_cvt_pk_bf16_f32 v85, v64, v65
	v_cvt_pk_bf16_f32 v86, v58, v59
	v_cvt_pk_bf16_f32 v87, v60, v61
	v_cvt_pk_bf16_f32 v88, v54, v55
	v_cvt_pk_bf16_f32 v89, v56, v57
	v_cvt_pk_bf16_f32 v90, v34, v35
	v_cvt_pk_bf16_f32 v91, v36, v37
	v_cvt_pk_bf16_f32 v92, v50, v51
	v_cvt_pk_bf16_f32 v93, v52, v53
	v_cvt_pk_bf16_f32 v94, v42, v43
	v_cvt_pk_bf16_f32 v95, v44, v45
	v_cvt_pk_bf16_f32 v96, v38, v39
	v_cvt_pk_bf16_f32 v97, v40, v41
	v_cvt_pk_bf16_f32 v98, v30, v31
	v_cvt_pk_bf16_f32 v99, v32, v33
	v_cvt_pk_bf16_f32 v100, v26, v27
	v_cvt_pk_bf16_f32 v101, v28, v29
	v_cvt_pk_bf16_f32 v102, v22, v23
	v_cvt_pk_bf16_f32 v103, v24, v25
	v_cvt_pk_bf16_f32 v104, v18, v19
	v_cvt_pk_bf16_f32 v105, v20, v21
	v_cvt_pk_bf16_f32 v106, v14, v15
	v_cvt_pk_bf16_f32 v107, v16, v17
	v_cvt_pk_bf16_f32 v108, v10, v11
	v_cvt_pk_bf16_f32 v109, v12, v13
	v_cvt_pk_bf16_f32 v110, v6, v7
	v_cvt_pk_bf16_f32 v111, v8, v9
	v_cvt_pk_bf16_f32 v112, v2, v3
	v_cvt_pk_bf16_f32 v113, v4, v5
	ds_read_b128 v[114:117], v247
	ds_read_b128 v[118:121], v247 offset:4096
	ds_read_b128 v[124:127], v247 offset:8192
	ds_read_b128 v[128:131], v247 offset:12288
	ds_read_b128 v[132:135], v247 offset:16384
	ds_read_b128 v[136:139], v247 offset:20480
	ds_read_b128 v[140:143], v247 offset:24576
	ds_read_b128 v[144:147], v247 offset:28672
	v_add_u32_e32 v148, 0x10000, v247
	v_add_u32_e32 v152, 0x10400, v247
	ds_read_b128 v[148:151], v148
	ds_read_b128 v[248:251], v152
	ds_read_b128 v[154:157], v247 offset:1024
	ds_read_b128 v[158:161], v247 offset:5120
	ds_read_b128 v[162:165], v247 offset:9216
	ds_read_b128 v[166:169], v247 offset:13312
	ds_read_b128 v[170:173], v247 offset:17408
	ds_read_b128 v[174:177], v247 offset:21504
	ds_read_b128 v[178:181], v247 offset:25600
	ds_read_b128 v[182:185], v247 offset:29696
	v_and_b32_e32 v153, 64, v244
	v_xor_b32_e32 v152, 16, v244
	v_add_u32_e32 v153, 64, v153
	v_cmp_lt_i32_e32 vcc, v152, v153
	v_add_u32_e32 v190, 0x10c00, v247
	v_add_u32_e32 v238, s86, v224
	v_cndmask_b32_e32 v152, v244, v152, vcc
	v_lshlrev_b32_e32 v225, 2, v152
	v_add_u32_e32 v152, 0x10800, v247
	ds_read_b128 v[186:189], v152
	ds_read_b128 v[190:193], v190
	v_xor_b32_e32 v152, 32, v244
	v_cmp_lt_i32_e32 vcc, v152, v153
	v_ashrrev_i32_e32 v239, 31, v238
	s_nop 0
	v_cndmask_b32_e32 v152, v244, v152, vcc
	v_lshlrev_b32_e32 v246, 2, v152
	s_waitcnt lgkmcnt(0)
	v_mfma_f32_16x16x32_bf16 v[114:117], v[82:85], v[114:117], 0
	v_mfma_f32_16x16x32_bf16 v[114:117], v[86:89], v[118:121], v[114:117]
	v_mfma_f32_16x16x32_bf16 v[114:117], v[90:93], v[124:127], v[114:117]
	v_mfma_f32_16x16x32_bf16 v[114:117], v[94:97], v[128:131], v[114:117]
	v_mfma_f32_16x16x32_bf16 v[114:117], v[98:101], v[132:135], v[114:117]
	v_mfma_f32_16x16x32_bf16 v[114:117], v[102:105], v[136:139], v[114:117]
	v_mfma_f32_16x16x32_bf16 v[114:117], v[106:109], v[140:143], v[114:117]
	v_mfma_f32_16x16x32_bf16 v[114:117], v[110:113], v[144:147], v[114:117]
	v_mfma_f32_16x16x32_bf16 v[114:117], v[78:81], v[148:151], v[114:117]
	v_mfma_f32_16x16x32_bf16 v[114:117], v[74:77], v[248:251], v[114:117]
	s_nop 7
	v_mul_f32_e32 v118, v115, v115
	v_mul_f32_e32 v119, v117, v117
	v_fmac_f32_e32 v118, v114, v114
	v_fmac_f32_e32 v119, v116, v116
	v_add_f32_e32 v124, v118, v119
	ds_bpermute_b32 v125, v225, v124
	ds_read_b128 v[118:121], v245
	s_waitcnt lgkmcnt(0)
	v_add_f32_e32 v124, v124, v125
	ds_bpermute_b32 v125, v246, v124
	s_waitcnt vmcnt(12)
	s_and_saveexec_b64 s[72:73], s[8:9]
	s_cbranch_execz .LBB0_559
	v_lshlrev_b64 v[126:127], 9, v[238:239]
	v_lshl_add_u64 v[126:127], s[70:71], 0, v[126:127]
	s_waitcnt lgkmcnt(0)
	v_add_f32_e32 v124, v124, v125
	global_store_dword v[126:127], v124, off

.LBB0_565:
	s_or_b64 exec, exec, s[72:73]
	v_lshlrev_b32_e32 v90, 16, v218
	s_waitcnt lgkmcnt(0)
	v_mul_f32_e32 v91, 0xbfb8aa3b, v90
	v_exp_f32_e32 v92, v91
	v_mov_b32_e32 v91, v86
	v_and_b32_e32 v86, 0xffff0000, v218
	v_mul_f32_e32 v93, 0xbfb8aa3b, v86
	v_exp_f32_e32 v94, v93
	v_mov_b32_e32 v93, v82
	v_add_f32_e32 v92, 1.0, v92
	v_rcp_f32_e32 v92, v92
	v_add_f32_e32 v82, 1.0, v94
	v_rcp_f32_e32 v82, v82
	v_add_u32_e32 v184, s2, v208
	v_pk_mul_f32 v[90:91], v[92:93], v[90:91]
	v_add_u32_e32 v128, 0x12000, v184
	v_pk_mul_f32 v[82:83], v[82:83], v[86:87]
	v_lshlrev_b32_e32 v86, 16, v219
	v_mul_f32_e32 v87, 0xbfb8aa3b, v86
	v_mul_f32_e32 v92, v90, v91
	v_exp_f32_e32 v90, v87
	v_mov_b32_e32 v87, v88
	v_and_b32_e32 v88, 0xffff0000, v219
	v_mul_f32_e32 v91, 0xbfb8aa3b, v88
	v_exp_f32_e32 v93, v91
	v_add_f32_e32 v90, 1.0, v90
	v_rcp_f32_e32 v90, v90
	v_mov_b32_e32 v91, v84
	v_add_f32_e32 v84, 1.0, v93
	v_rcp_f32_e32 v84, v84
	v_mul_f32_e32 v93, v82, v83
	v_pk_mul_f32 v[82:83], v[90:91], v[86:87]
	s_nop 0
	v_mul_f32_e32 v86, v82, v83
	v_pk_mul_f32 v[82:83], v[84:85], v[88:89]
	v_add_co_u32_e32 v84, vcc, s76, v240
	v_mul_f32_e32 v83, v82, v83
	v_cvt_pk_bf16_f32 v82, v92, v93
	v_cvt_pk_bf16_f32 v83, v86, v83
	s_nop 0
	v_addc_co_u32_e32 v85, vcc, 0, v241, vcc
	global_store_dwordx2 v[84:85], v[82:83], off
	v_lshl_add_u64 v[82:83], s[14:15], 0, v[232:233]
	v_add_co_u32_e32 v84, vcc, s77, v82
	s_nop 1
	v_addc_co_u32_e32 v85, vcc, 0, v83, vcc
	v_add_co_u32_e32 v86, vcc, s78, v82
	s_nop 1
	v_addc_co_u32_e32 v87, vcc, 0, v83, vcc
	v_add_co_u32_e32 v88, vcc, s79, v82
	s_nop 1
	v_addc_co_u32_e32 v89, vcc, 0, v83, vcc
	v_add_co_u32_e32 v82, vcc, s80, v82
	s_nop 1
	v_addc_co_u32_e32 v83, vcc, 0, v83, vcc
	global_load_dwordx2 v[122:123], v[84:85], off
	global_load_dwordx2 v[236:237], v[86:87], off
	global_load_dwordx2 v[220:221], v[88:89], off
	global_load_dwordx2 v[218:219], v[82:83], off
	ds_read_b128 v[82:85], v247 offset:32768
	ds_read_b128 v[86:89], v247 offset:33792
	ds_read_b128 v[90:93], v247 offset:34816
	ds_read_b128 v[94:97], v247 offset:35840
	ds_read_b128 v[98:101], v247 offset:36864
	ds_read_b128 v[102:105], v247 offset:37888
	ds_read_b128 v[106:109], v247 offset:38912
	ds_read_b128 v[110:113], v247 offset:39936
	ds_read_b128 v[114:117], v128
	ds_read_b128 v[118:121], v128 offset:64
	ds_read_b128 v[124:127], v128 offset:128
	ds_read_b128 v[128:131], v128 offset:192
	ds_read_b128 v[132:135], v247 offset:40960
	ds_read_b128 v[136:139], v247 offset:41984
	ds_read_b128 v[140:143], v247 offset:43008
	ds_read_b128 v[144:147], v247 offset:44032
	ds_read_b128 v[148:151], v247 offset:45056
	ds_read_b128 v[152:155], v247 offset:46080
	ds_read_b128 v[156:159], v247 offset:47104
	ds_read_b128 v[160:163], v247 offset:48128
	v_add_u32_e32 v164, 0x12100, v184
	v_add_u32_e32 v168, 0x12140, v184
	v_add_u32_e32 v172, 0x12180, v184
	v_add_u32_e32 v176, 0x121c0, v184
	ds_read_b128 v[164:167], v164
	ds_read_b128 v[168:171], v168
	ds_read_b128 v[172:175], v172
	ds_read_b128 v[176:179], v176
	s_waitcnt lgkmcnt(0)
	v_pk_mul_f32 v[48:49], v[48:49], v[116:117]
	v_pk_mul_f32 v[46:47], v[46:47], v[114:115]
	v_pk_mul_f32 v[64:65], v[64:65], v[120:121]
	v_pk_mul_f32 v[62:63], v[62:63], v[118:119]
	v_mfma_f32_16x16x32_bf16 v[46:49], v[82:85], v[78:81], v[46:49]
	v_mul_f32_e64 v60, v60, v126
	v_mul_f32_e64 v61, v61, v127
	v_pk_mul_f32 v[58:59], v[58:59], v[124:125]
	v_pk_mul_f32 v[56:57], v[56:57], v[130:131]
	v_mfma_f32_16x16x32_bf16 v[62:65], v[90:93], v[78:81], v[62:65]
	v_mul_f32_e64 v54, v54, v128
	v_mul_f32_e64 v55, v55, v129
	v_add_u32_e32 v128, 0x12200, v184
	v_add_u32_e32 v129, 0x12240, v184
	v_mfma_f32_16x16x32_bf16 v[58:61], v[98:101], v[78:81], v[58:61]
	v_add_u32_e32 v180, 0x122c0, v184
	v_mfma_f32_16x16x32_bf16 v[54:57], v[106:109], v[78:81], v[54:57]
	v_add_u32_e32 v106, 0x12280, v184
	v_mfma_f32_16x16x32_bf16 v[46:49], v[86:89], v[74:77], v[46:49]
	ds_read_b128 v[82:85], v247 offset:49152
	ds_read_b128 v[86:89], v247 offset:50176
	v_mfma_f32_16x16x32_bf16 v[62:65], v[94:97], v[74:77], v[62:65]
	ds_read_b128 v[90:93], v247 offset:51200
	ds_read_b128 v[94:97], v247 offset:52224
	ds_read_b128 v[114:117], v247 offset:53248
	ds_read_b128 v[118:121], v247 offset:54272
	ds_read_b128 v[98:101], v247 offset:55296
	ds_read_b128 v[124:127], v247 offset:56320
	v_mfma_f32_16x16x32_bf16 v[58:61], v[102:105], v[74:77], v[58:61]
	ds_read_b128 v[102:105], v128
	ds_read_b128 v[128:131], v129
	ds_read_b128 v[106:109], v106
	ds_read_b128 v[180:183], v180
	v_mfma_f32_16x16x32_bf16 v[54:57], v[110:113], v[74:77], v[54:57]
	v_mul_f32_e64 v36, v36, v166
	v_mul_f32_e64 v37, v37, v167
	v_pk_mul_f32 v[34:35], v[34:35], v[164:165]
	v_pk_mul_f32 v[52:53], v[52:53], v[170:171]
	v_pk_mul_f32 v[50:51], v[50:51], v[168:169]
	v_mfma_f32_16x16x32_bf16 v[34:37], v[132:135], v[78:81], v[34:37]
	v_mul_f32_e64 v44, v44, v174
	v_mul_f32_e64 v45, v45, v175
	v_pk_mul_f32 v[42:43], v[42:43], v[172:173]
	v_pk_mul_f32 v[40:41], v[40:41], v[178:179]
	v_mfma_f32_16x16x32_bf16 v[50:53], v[140:143], v[78:81], v[50:53]
	v_mul_f32_e64 v38, v38, v176
	v_mul_f32_e64 v39, v39, v177
	ds_read_b128 v[110:113], v247 offset:57344
	ds_read_b128 v[132:135], v247 offset:58368
	v_add_u32_e32 v172, 0x12300, v184
	v_mfma_f32_16x16x32_bf16 v[42:45], v[148:151], v[78:81], v[42:45]
	v_add_u32_e32 v173, 0x12340, v184
	v_add_u32_e32 v176, 0x123c0, v184
	v_mfma_f32_16x16x32_bf16 v[38:41], v[156:159], v[78:81], v[38:41]
	v_add_u32_e32 v156, 0x12380, v184
	v_mfma_f32_16x16x32_bf16 v[34:37], v[136:139], v[74:77], v[34:37]
	v_mfma_f32_16x16x32_bf16 v[50:53], v[144:147], v[74:77], v[50:53]
	ds_read_b128 v[136:139], v247 offset:59392
	ds_read_b128 v[140:143], v247 offset:60416
	ds_read_b128 v[144:147], v247 offset:61440
	ds_read_b128 v[164:167], v247 offset:62464
	ds_read_b128 v[148:151], v247 offset:63488
	ds_read_b128 v[168:171], v247 offset:64512
	v_mfma_f32_16x16x32_bf16 v[42:45], v[152:155], v[74:77], v[42:45]
	ds_read_b128 v[152:155], v172
	ds_read_b128 v[172:175], v173
	ds_read_b128 v[156:159], v156
	ds_read_b128 v[176:179], v176
	v_mfma_f32_16x16x32_bf16 v[38:41], v[160:163], v[74:77], v[38:41]
	s_waitcnt lgkmcnt(0)
	v_pk_mul_f32 v[32:33], v[32:33], v[104:105]
	v_pk_mul_f32 v[30:31], v[30:31], v[102:103]
	v_pk_mul_f32 v[28:29], v[28:29], v[130:131]
	v_pk_mul_f32 v[26:27], v[26:27], v[128:129]
	v_pk_mul_f32 v[24:25], v[24:25], v[108:109]
	v_pk_mul_f32 v[22:23], v[22:23], v[106:107]
	v_pk_mul_f32 v[20:21], v[20:21], v[182:183]
	v_pk_mul_f32 v[18:19], v[18:19], v[180:181]
	v_mfma_f32_16x16x32_bf16 v[30:33], v[82:85], v[78:81], v[30:33]
	v_mfma_f32_16x16x32_bf16 v[26:29], v[90:93], v[78:81], v[26:29]
	v_mfma_f32_16x16x32_bf16 v[22:25], v[114:117], v[78:81], v[22:25]
	v_mfma_f32_16x16x32_bf16 v[18:21], v[98:101], v[78:81], v[18:21]
	v_mfma_f32_16x16x32_bf16 v[30:33], v[86:89], v[74:77], v[30:33]
	v_mfma_f32_16x16x32_bf16 v[26:29], v[94:97], v[74:77], v[26:29]
	v_mfma_f32_16x16x32_bf16 v[22:25], v[118:121], v[74:77], v[22:25]
	v_mfma_f32_16x16x32_bf16 v[18:21], v[124:127], v[74:77], v[18:21]
	v_mul_f32_e64 v16, v16, v154
	v_mul_f32_e64 v17, v17, v155
	v_pk_mul_f32 v[14:15], v[14:15], v[152:153]
	v_pk_mul_f32 v[12:13], v[12:13], v[174:175]
	v_pk_mul_f32 v[10:11], v[10:11], v[172:173]
	v_pk_mul_f32 v[8:9], v[8:9], v[158:159]
	v_pk_mul_f32 v[6:7], v[6:7], v[156:157]
	v_pk_mul_f32 v[4:5], v[4:5], v[178:179]
	v_pk_mul_f32 v[2:3], v[2:3], v[176:177]
	v_mfma_f32_16x16x32_bf16 v[14:17], v[110:113], v[78:81], v[14:17]
	s_add_i32 s86, s86, 64
	v_lshl_add_u64 v[226:227], v[226:227], 0, s[28:29]
	v_lshl_add_u64 v[228:229], v[228:229], 0, s[62:63]
	v_mfma_f32_16x16x32_bf16 v[10:13], v[136:139], v[78:81], v[10:13]
	v_lshl_add_u64 v[230:231], v[230:231], 0, s[64:65]
	v_lshl_add_u64 v[232:233], v[232:233], 0, s[66:67]
	v_lshl_add_u64 v[234:235], v[234:235], 0, s[68:69]
	v_mfma_f32_16x16x32_bf16 v[6:9], v[144:147], v[78:81], v[6:9]
	s_cmpk_eq_i32 s86, 0x7c0
	v_mfma_f32_16x16x32_bf16 v[2:5], v[148:151], v[78:81], v[2:5]
	v_mfma_f32_16x16x32_bf16 v[14:17], v[132:135], v[74:77], v[14:17]
	v_mfma_f32_16x16x32_bf16 v[10:13], v[140:143], v[74:77], v[10:13]
	v_mfma_f32_16x16x32_bf16 v[6:9], v[164:167], v[74:77], v[6:9]
	v_mfma_f32_16x16x32_bf16 v[2:5], v[168:171], v[74:77], v[2:5]
	s_cbranch_scc1 .LBB0_567
	s_waitcnt vmcnt(12)
	v_mov_b64_e32 v[80:81], v[72:73]
	v_mov_b64_e32 v[76:77], v[68:69]
	v_mov_b64_e32 v[78:79], v[70:71]
	v_mov_b64_e32 v[74:75], v[66:67]
	s_mov_b32 s2, s22
	s_branch .LBB0_555
